# HGRN2 chunk loops (phases 2 and 4): next item's loads stay in flight during the item (conversions and waits moved to the item end)
# speedup vs baseline: 1.0003x; 1.0003x over previous
; #define GAS __attribute__((address_space(1)))
; __device__ __forceinline__ unsigned pk2(float lo, float hi) { return f2bf(lo) | (f2bf(hi) << 16); }
; __device__ __forceinline__ f32x4 mfma16(bf16x8 a, bf16x8 b, f32x4 c) { return __builtin_amdgcn_mfma_f32_16x16x32_bf16(a, b, c, 0, 0, 0); }
; __device__ __forceinline__ s16x4 tr_read(unsigned lds_addr) { s16x4 r; asm volatile("ds_read_b64_tr_b16 %0, %1\n\ts_waitcnt lgkmcnt(0)" : "=&v"(r) : "v"(lds_addr) : "memory"); return r; }
; __device__ __forceinline__ void h1_item(Frame& F, int chunk, int tid, const H1Regs& R) {
;     ...
;     const unsigned ktb = (unsigned)(size_t)KT, vtb = (unsigned)(size_t)VT;
;     const int q = i >> 2, p4 = i & 3;
;     bf16x8 af[2];
; #pragma unroll
;     for (int ks = 0; ks < 2; ++ks) { const s16x4 lo = tr_read(ktb + (32 * ks + 8 * g + q) * TROW + (16 * w + 4 * p4) * 2), hi = tr_read(ktb + (32 * ks + 8 * g + 4 + q) * TROW + (16 * w + 4 * p4) * 2);
;         af[ks] = (bf16x8){lo[0], lo[1], lo[2], lo[3], hi[0], hi[1], hi[2], hi[3]}; }
;     f32x4 uacc[8];
; #pragma unroll
;     for (int vb = 0; vb < 8; ++vb) uacc[vb] = (f32x4){0.f, 0.f, 0.f, 0.f};
; #pragma unroll
;     for (int ks = 0; ks < 2; ++ks) { s16x4 lo[8], hi[8];
;         tr_read8<32>(lo, vtb + (32 * ks + 8 * g + q) * TROW + 8 * p4); tr_read8<32>(hi, vtb + (32 * ks + 8 * g + 4 + q) * TROW + 8 * p4);
; #pragma unroll
;         for (int vb = 0; vb < 8; ++vb) uacc[vb] = mfma16(af[ks], TRCAT(lo[vb], hi[vb]), uacc[vb]); }
; #pragma unroll
;     for (int vb = 0; vb < 8; ++vb) { u32x2 wv; wv.x = pk2(uacc[vb][0], uacc[vb][1]); wv.y = pk2(uacc[vb][2], uacc[vb][3]);
;         *(GAS u32x2*)((GAS bf16_t*)UT + (size_t)chunk * 16384 + (16 * vb + i) * 128 + 16 * w + 4 * g) = wv; }
.LBB0_730:
	s_or_b64 exec, exec, s[30:31]
	s_ashr_i32 s22, s22, 6
	v_lshl_or_b32 v10, s22, 5, v20
	s_waitcnt lgkmcnt(0)
	s_barrier
	v_add_u32_e32 v14, s0, v10
	v_add_u32_e32 v16, s1, v10
	v_add_u32_e32 v12, v14, v34
	ds_read_b64_tr_b16 v[10:11], v12
	s_waitcnt lgkmcnt(0)
	v_add_u32_e32 v15, v16, v34
	ds_read_b64_tr_b16 v[12:13], v15
	s_waitcnt lgkmcnt(0)
	v_add_u32_e32 v17, v14, v35
	ds_read_b64_tr_b16 v[14:15], v17
	s_waitcnt lgkmcnt(0)
	v_add_u32_e32 v58, v16, v35
	ds_read_b64_tr_b16 v[16:17], v58
	s_waitcnt lgkmcnt(0)
	ds_read_b64_tr_b16 v[86:87], v36
	ds_read_b64_tr_b16 v[82:83], v36 offset:32
	ds_read_b64_tr_b16 v[78:79], v36 offset:64
	ds_read_b64_tr_b16 v[74:75], v36 offset:0x60
	ds_read_b64_tr_b16 v[70:71], v36 offset:0x80
	ds_read_b64_tr_b16 v[66:67], v36 offset:0xa0
	ds_read_b64_tr_b16 v[62:63], v36 offset:0xc0
	ds_read_b64_tr_b16 v[58:59], v36 offset:0xe0
	s_waitcnt lgkmcnt(0)
	ds_read_b64_tr_b16 v[88:89], v37
	ds_read_b64_tr_b16 v[84:85], v37 offset:32
	ds_read_b64_tr_b16 v[80:81], v37 offset:64
	ds_read_b64_tr_b16 v[76:77], v37 offset:0x60
	ds_read_b64_tr_b16 v[72:73], v37 offset:0x80
	ds_read_b64_tr_b16 v[68:69], v37 offset:0xa0
	ds_read_b64_tr_b16 v[64:65], v37 offset:0xc0
	ds_read_b64_tr_b16 v[60:61], v37 offset:0xe0
	s_waitcnt lgkmcnt(0)
	ds_read_b64_tr_b16 v[118:119], v38
	ds_read_b64_tr_b16 v[114:115], v38 offset:32
	ds_read_b64_tr_b16 v[110:111], v38 offset:64
	ds_read_b64_tr_b16 v[106:107], v38 offset:0x60
	ds_read_b64_tr_b16 v[102:103], v38 offset:0x80
	ds_read_b64_tr_b16 v[98:99], v38 offset:0xa0
	ds_read_b64_tr_b16 v[94:95], v38 offset:0xc0
	ds_read_b64_tr_b16 v[90:91], v38 offset:0xe0
	s_waitcnt lgkmcnt(0)
	ds_read_b64_tr_b16 v[120:121], v39
	ds_read_b64_tr_b16 v[116:117], v39 offset:32
	ds_read_b64_tr_b16 v[112:113], v39 offset:64
	ds_read_b64_tr_b16 v[108:109], v39 offset:0x60
	ds_read_b64_tr_b16 v[104:105], v39 offset:0x80
	ds_read_b64_tr_b16 v[100:101], v39 offset:0xa0
	ds_read_b64_tr_b16 v[96:97], v39 offset:0xc0
	ds_read_b64_tr_b16 v[92:93], v39 offset:0xe0
	s_waitcnt lgkmcnt(0)
	s_lshl_b32 s30, s22, 4
	v_mfma_f32_16x16x32_bf16 v[86:89], v[10:13], v[86:89], 0
	s_ashr_i32 s31, s30, 31
	s_add_i32 s40, s40, s18
	s_lshl_b64 s[30:31], s[30:31], 1
	v_mfma_f32_16x16x32_bf16 v[86:89], v[14:17], v[118:121], v[86:89]
	s_add_u32 s30, s16, s30
	s_addc_u32 s31, s17, s31
	s_add_i32 s3, s3, s19
	v_mfma_f32_16x16x32_bf16 v[82:85], v[10:13], v[82:85], 0
	s_add_i32 s21, s21, s24
	s_nop 2
	v_bfe_u32 v118, v86, 16, 1
	v_add3_u32 v86, v86, v118, s34
	v_bfe_u32 v118, v87, 16, 1
	v_mfma_f32_16x16x32_bf16 v[78:81], v[10:13], v[78:81], 0
	v_lshrrev_b32_e32 v86, 16, v86
	s_add_i32 s25, s25, s33
	s_add_i32 s2, s2, s18
	v_mfma_f32_16x16x32_bf16 v[74:77], v[10:13], v[74:77], 0
	v_lshl_add_u64 v[26:27], v[26:27], 0, s[26:27]
	s_cmpk_lt_i32 s40, 0x800
	v_mfma_f32_16x16x32_bf16 v[70:73], v[10:13], v[70:73], 0
	v_mfma_f32_16x16x32_bf16 v[66:69], v[10:13], v[66:69], 0
	v_mfma_f32_16x16x32_bf16 v[62:65], v[10:13], v[62:65], 0
	v_mfma_f32_16x16x32_bf16 v[10:13], v[10:13], v[58:61], 0
	v_add3_u32 v58, v87, v118, s34
	v_bfe_u32 v87, v88, 16, 1
	v_and_or_b32 v86, v58, s35, v86
	v_mfma_f32_16x16x32_bf16 v[58:61], v[14:17], v[114:117], v[82:85]
	s_nop 2
	v_add3_u32 v82, v88, v87, s34
	v_bfe_u32 v83, v89, 16, 1
	v_lshrrev_b32_e32 v82, 16, v82
	v_add3_u32 v83, v89, v83, s34
	v_and_or_b32 v87, v83, s35, v82
	v_lshl_add_u64 v[82:83], s[30:31], 0, v[28:29]
	v_add_co_u32_e32 v84, vcc, s36, v82
	v_mfma_f32_16x16x32_bf16 v[78:81], v[14:17], v[110:113], v[78:81]
	s_nop 0
	v_addc_co_u32_e32 v85, vcc, 0, v83, vcc
	global_store_dwordx2 v[84:85], v[86:87], off offset:-4096
	v_mfma_f32_16x16x32_bf16 v[74:77], v[14:17], v[106:109], v[74:77]
	v_bfe_u32 v86, v58, 16, 1
	v_add3_u32 v58, v58, v86, s34
	v_bfe_u32 v86, v59, 16, 1
	v_mfma_f32_16x16x32_bf16 v[70:73], v[14:17], v[102:105], v[70:73]
	v_lshrrev_b32_e32 v58, 16, v58
	v_add3_u32 v59, v59, v86, s34
	v_and_or_b32 v58, v59, s35, v58
	v_mfma_f32_16x16x32_bf16 v[66:69], v[14:17], v[98:101], v[66:69]
	v_lshl_add_u64 v[28:29], v[28:29], 0, s[28:29]
	v_mfma_f32_16x16x32_bf16 v[62:65], v[14:17], v[94:97], v[62:65]
	v_mfma_f32_16x16x32_bf16 v[10:13], v[14:17], v[90:93], v[10:13]
	v_bfe_u32 v14, v60, 16, 1
	v_add3_u32 v14, v60, v14, s34
	v_bfe_u32 v15, v61, 16, 1
	v_lshrrev_b32_e32 v14, 16, v14
	v_add3_u32 v15, v61, v15, s34
	v_and_or_b32 v59, v15, s35, v14
	v_bfe_u32 v14, v78, 16, 1
	v_add3_u32 v14, v78, v14, s34
	v_bfe_u32 v15, v79, 16, 1
	v_lshrrev_b32_e32 v14, 16, v14
	v_add3_u32 v15, v79, v15, s34
	v_and_or_b32 v14, v15, s35, v14
	v_bfe_u32 v15, v80, 16, 1
	v_add3_u32 v15, v80, v15, s34
	v_bfe_u32 v16, v81, 16, 1
	v_lshrrev_b32_e32 v15, 16, v15
	v_add3_u32 v16, v81, v16, s34
	v_and_or_b32 v15, v16, s35, v15
	v_add_co_u32_e32 v16, vcc, s37, v82
	global_store_dwordx2 v[84:85], v[58:59], off
	s_nop 0
	v_addc_co_u32_e32 v17, vcc, 0, v83, vcc
	global_store_dwordx2 v[16:17], v[14:15], off offset:-4096
	v_bfe_u32 v14, v74, 16, 1
	v_add3_u32 v14, v74, v14, s34
	v_bfe_u32 v15, v75, 16, 1
	v_lshrrev_b32_e32 v14, 16, v14
	v_add3_u32 v15, v75, v15, s34
	v_and_or_b32 v14, v15, s35, v14
	v_bfe_u32 v15, v76, 16, 1
	v_add3_u32 v15, v76, v15, s34
	v_bfe_u32 v58, v77, 16, 1
	v_lshrrev_b32_e32 v15, 16, v15
	v_add3_u32 v58, v77, v58, s34
	v_and_or_b32 v15, v58, s35, v15
	global_store_dwordx2 v[16:17], v[14:15], off
	v_bfe_u32 v14, v70, 16, 1
	v_add3_u32 v14, v70, v14, s34
	v_bfe_u32 v15, v71, 16, 1
	v_lshrrev_b32_e32 v14, 16, v14
	v_add3_u32 v15, v71, v15, s34
	v_and_or_b32 v14, v15, s35, v14
	v_bfe_u32 v15, v72, 16, 1
	v_add3_u32 v15, v72, v15, s34
	v_bfe_u32 v16, v73, 16, 1
	v_lshrrev_b32_e32 v15, 16, v15
	v_add3_u32 v16, v73, v16, s34
	v_and_or_b32 v15, v16, s35, v15
	v_add_co_u32_e32 v16, vcc, s38, v82
	v_bfe_u32 v58, v69, 16, 1
	s_nop 0
	v_addc_co_u32_e32 v17, vcc, 0, v83, vcc
	global_store_dwordx2 v[16:17], v[14:15], off offset:-4096
	v_bfe_u32 v14, v66, 16, 1
	v_add3_u32 v14, v66, v14, s34
	v_bfe_u32 v15, v67, 16, 1
	v_lshrrev_b32_e32 v14, 16, v14
	v_add3_u32 v15, v67, v15, s34
	v_and_or_b32 v14, v15, s35, v14
	v_bfe_u32 v15, v68, 16, 1
	v_add3_u32 v15, v68, v15, s34
	v_lshrrev_b32_e32 v15, 16, v15
	v_add3_u32 v58, v69, v58, s34
	v_and_or_b32 v15, v58, s35, v15
	global_store_dwordx2 v[16:17], v[14:15], off
	v_bfe_u32 v14, v62, 16, 1
	v_add3_u32 v14, v62, v14, s34
	v_bfe_u32 v15, v63, 16, 1
	v_lshrrev_b32_e32 v14, 16, v14
	v_add3_u32 v15, v63, v15, s34
	v_and_or_b32 v14, v15, s35, v14
	v_bfe_u32 v15, v64, 16, 1
	v_add3_u32 v15, v64, v15, s34
	v_bfe_u32 v16, v65, 16, 1
	v_lshrrev_b32_e32 v15, 16, v15
	v_add3_u32 v16, v65, v16, s34
	v_and_or_b32 v15, v16, s35, v15
	v_add_co_u32_e32 v16, vcc, s39, v82
	s_waitcnt vmcnt(6)
; #define GAS __attribute__((address_space(1)))
; #define LDS_BARRIER() asm volatile("s_waitcnt lgkmcnt(0)\n\ts_barrier" ::: "memory")
; __device__ __forceinline__ unsigned pk2(float lo, float hi) { return f2bf(lo) | (f2bf(hi) << 16); }
; __device__ __forceinline__ void h1_load(Frame& F, int chunk, int tid, H1Regs& R) {
;     const GAS bf16_t* H = (const GAS bf16_t*)(F.ws + WS_H); const GAS _Float16* LF = (const GAS _Float16*)(F.ws + WS_LF);
;     const int bh = chunk >> 5, n = chunk & 31, b = bh >> 3, head = bh & 7, tok0 = b * SEQ + n * 64, kk = tid & 127, part = tid >> 7;
;     const GAS _Float16* p = LF + HOFF(head * 128, tok0 + part * 16) + kk;
; #pragma unroll
;     for (int j = 0; j < 16; ++j) R.lf[j] = (float)p[(size_t)j * 128];
; #pragma unroll
;     for (int j = 0; j < 2; ++j) { const int c = tid + 512 * j, row = c >> 4, ch = c & 15;
;         R.v[j] = *(const GAS u32x4*)(H + HOFF(C_HI + head * 128, tok0 + row) + ch * 8); }
; }
; __device__ __forceinline__ void h1_item(Frame& F, int chunk, int tid, const H1Regs& R) {
;     ...
;     for (int vb = 0; vb < 8; ++vb) { u32x2 wv; wv.x = pk2(uacc[vb][0], uacc[vb][1]); wv.y = pk2(uacc[vb][2], uacc[vb][3]);
;         *(GAS u32x2*)((GAS bf16_t*)UT + (size_t)chunk * 16384 + (16 * vb + i) * 128 + 16 * w + 4 * g) = wv; }
;     LDS_BARRIER();
	v_cvt_f32_f16_e32 v57, v176
	v_cvt_f32_f16_e32 v56, v177
	v_cvt_f32_f16_e32 v55, v178
	v_cvt_f32_f16_e32 v54, v179
	v_cvt_f32_f16_e32 v53, v180
	v_cvt_f32_f16_e32 v52, v181
	v_cvt_f32_f16_e32 v51, v182
	v_cvt_f32_f16_e32 v50, v183
	v_cvt_f32_f16_e32 v49, v184
	v_cvt_f32_f16_e32 v48, v185
	v_cvt_f32_f16_e32 v47, v186
	v_cvt_f32_f16_e32 v46, v187
	v_cvt_f32_f16_e32 v45, v188
	v_cvt_f32_f16_e32 v44, v189
	v_cvt_f32_f16_e32 v43, v190
	v_cvt_f32_f16_e32 v42, v191
	v_mov_b32_e32 v58, v42
	s_nop 0
	v_addc_co_u32_e32 v17, vcc, 0, v83, vcc
	global_store_dwordx2 v[16:17], v[14:15], off
	v_bfe_u32 v14, v10, 16, 1
	v_add3_u32 v10, v10, v14, s34
	v_bfe_u32 v14, v11, 16, 1
	v_lshrrev_b32_e32 v10, 16, v10
	v_add3_u32 v11, v11, v14, s34
	v_and_or_b32 v10, v11, s35, v10
	v_bfe_u32 v11, v12, 16, 1
	v_add3_u32 v11, v12, v11, s34
	v_bfe_u32 v12, v13, 16, 1
	v_lshrrev_b32_e32 v11, 16, v11
	v_add3_u32 v12, v13, v12, s34
	v_and_or_b32 v11, v12, s35, v11
	v_add_co_u32_e32 v12, vcc, 0x5cb07000, v82
	v_mov_b64_e32 v[16:17], v[8:9]
	s_nop 0
	v_addc_co_u32_e32 v13, vcc, 0, v83, vcc
	global_store_dwordx2 v[12:13], v[10:11], off
	s_waitcnt lgkmcnt(0)
	s_barrier
	v_mov_b64_e32 v[12:13], v[4:5]
	v_mov_b64_e32 v[10:11], v[2:3]
	v_mov_b64_e32 v[14:15], v[6:7]
	v_mov_b32_e32 v59, v43
	v_mov_b32_e32 v60, v44
	v_mov_b32_e32 v61, v45
	v_mov_b32_e32 v62, v46
	v_mov_b32_e32 v63, v47
	v_mov_b32_e32 v64, v48
	v_mov_b32_e32 v65, v49
	v_mov_b32_e32 v66, v50
	v_mov_b32_e32 v67, v51
	v_mov_b32_e32 v68, v52
	v_mov_b32_e32 v69, v53
	v_mov_b32_e32 v70, v54
	v_mov_b32_e32 v71, v55
	v_mov_b32_e32 v72, v56
	v_mov_b32_e32 v73, v57
	s_cbranch_scc0 .LBB0_735
.LBB0_731:
	s_cmpk_gt_i32 s2, 0x7ff
	s_cbranch_scc1 .Lpfdrain_h1L0
	s_and_b32 s22, s3, 0xfffff800
	s_and_b32 s30, s21, 0x7c0
	s_or_b32 s30, s22, s30
	v_add_u32_e32 v2, s30, v1
	s_and_b32 s22, s25, 0x1c000
	v_ashrrev_i32_e32 v3, 31, v2
	v_lshl_add_u64 v[2:3], v[2:3], 0, s[22:23]
	v_lshlrev_b64 v[2:3], 8, v[2:3]
	v_lshl_add_u64 v[2:3], v[24:25], 0, v[2:3]
	global_load_ushort v176, v[2:3], off
	global_load_ushort v177, v[2:3], off offset:256
	global_load_ushort v178, v[2:3], off offset:512
	global_load_ushort v179, v[2:3], off offset:768
	global_load_ushort v180, v[2:3], off offset:1024
	global_load_ushort v181, v[2:3], off offset:1280
	global_load_ushort v182, v[2:3], off offset:1536
	global_load_ushort v183, v[2:3], off offset:1792
	global_load_ushort v184, v[2:3], off offset:2048
	global_load_ushort v185, v[2:3], off offset:2304
	global_load_ushort v186, v[2:3], off offset:2560
	global_load_ushort v187, v[2:3], off offset:2816
	global_load_ushort v188, v[2:3], off offset:3072
	global_load_ushort v189, v[2:3], off offset:3328
	global_load_ushort v190, v[2:3], off offset:3584
	global_load_ushort v191, v[2:3], off offset:3840
	v_add_u32_e32 v2, s30, v30
	v_add_u32_e32 v4, s30, v31
	s_bitset1_b32 s22, 18
	v_ashrrev_i32_e32 v3, 31, v2
	v_ashrrev_i32_e32 v5, 31, v4
	v_lshl_add_u64 v[2:3], v[2:3], 0, s[22:23]
	v_lshl_add_u64 v[4:5], v[4:5], 0, s[22:23]
	v_lshlrev_b64 v[2:3], 8, v[2:3]
	v_lshlrev_b64 v[4:5], 8, v[4:5]
	v_lshl_add_u64 v[2:3], v[22:23], 0, v[2:3]
	v_lshl_add_u64 v[4:5], v[22:23], 0, v[4:5]
	global_load_dwordx4 v[6:9], v[2:3], off
	s_nop 0
	global_load_dwordx4 v[2:5], v[4:5], off
	s_waitcnt vmcnt(18)
	s_branch .LBB0_733

; #define GAS __attribute__((address_space(1)))
; #define LAS __attribute__((address_space(3)))
; #define LDS_BARRIER() asm volatile("s_waitcnt lgkmcnt(0)\n\ts_barrier" ::: "memory")
; __device__ __forceinline__ unsigned cvt_pk_bf16(float lo, float hi) { unsigned r; asm volatile("v_cvt_pk_bf16_f32 %0, %1, %2" : "=v"(r) : "v"(lo), "v"(hi)); return r; }
; __device__ __forceinline__ void h1_item(Frame& F, int chunk, int tid, const H1Regs& R) {
;     GAS float* UT = (GAS float*)(F.ws + WS_UT); GAS float* DEC = (GAS float*)(F.ws + WS_DEC);
;     LAS unsigned char* KT = F.lds; LAS unsigned char* VT = F.lds + 17408; LAS float* TOT = (LAS float*)(F.lds + 34816);
;     const int lane = tid & 63, w = __builtin_amdgcn_readfirstlane(tid >> 6);
;     const int kk = tid & 127, part = tid >> 7, g = lane >> 4, i = lane & 15;
;     float lf[16], cum[16];
; #pragma unroll
;     for (int j = 0; j < 16; ++j) lf[j] = R.lf[j];
; #pragma unroll
;     for (int j = 0; j < 2; ++j) { const int c = tid + 512 * j, row = c >> 4, ch = c & 15; *(LAS u32x4*)(VT + row * TROW + ch * 16) = R.v[j]; }
;     float run = 0.f;
; #pragma unroll
;     for (int j = 0; j < 16; ++j) { run += lf[j]; cum[j] = run; }
;     TOT[part * 128 + kk] = run;
;     LDS_BARRIER();
;     float off = 0.f, end = 0.f;
; #pragma unroll
;     for (int p = 0; p < 4; ++p) { const float t = TOT[p * 128 + kk]; if (p < part) off += t; end += t; }
; #pragma unroll
;     for (int j = 0; j < 16; ++j) { const float c = cum[j] + off; const float kt = (1.0f - __expf(lf[j])) * __expf(end - c);
;         *(LAS unsigned short*)(KT + (part * 16 + j) * TROW + kk * 2) = (unsigned short)cvt_pk_bf16(kt, 0.f); }
;     if (part == 0) DEC[(size_t)chunk * 128 + kk] = __expf(end);
.LBB0_733:
	ds_write_b128 v19, v[14:17] offset:17408
	ds_write_b128 v40, v[10:13] offset:17408
	v_add_f32_e32 v14, 0, v73
	v_add_f32_e32 v15, v72, v14
	v_add_f32_e32 v16, v71, v15
	v_add_f32_e32 v17, v70, v16
	v_add_f32_e32 v74, v69, v17
	v_add_f32_e32 v75, v68, v74
	v_add_f32_e32 v76, v67, v75
	v_add_f32_e32 v77, v66, v76
	v_add_f32_e32 v78, v65, v77
	v_add_f32_e32 v79, v64, v78
	v_add_f32_e32 v80, v63, v79
	v_add_f32_e32 v81, v62, v80
	v_add_f32_e32 v82, v61, v81
	v_add_f32_e32 v83, v60, v82
	v_add_f32_e32 v84, v59, v83
	v_add_f32_e32 v85, v58, v84
	ds_write_b32 v32, v85 offset:34816
	s_waitcnt lgkmcnt(0)
	s_barrier
	ds_read2st64_b32 v[10:11], v33 offset0:136 offset1:138
	ds_read2st64_b32 v[12:13], v33 offset0:140 offset1:142
	v_readfirstlane_b32 s22, v18
	s_waitcnt lgkmcnt(1)
	v_add_f32_e32 v10, 0, v10
	v_cndmask_b32_e64 v86, 0, v10, s[4:5]
	v_add_f32_e32 v10, v10, v11
	v_add_f32_e32 v11, v11, v86
	v_cndmask_b32_e64 v11, v86, v11, s[6:7]
	s_waitcnt lgkmcnt(0)
	v_add_f32_e32 v86, v12, v11
	v_cndmask_b32_e64 v11, v11, v86, s[8:9]
	v_add_f32_e32 v10, v10, v12
	v_add_f32_e32 v12, v13, v11
	v_cndmask_b32_e64 v11, v11, v12, s[10:11]
	v_add_f32_e32 v10, v10, v13
	v_add_f32_e32 v12, v14, v11
	v_mul_f32_e32 v13, 0x3fb8aa3b, v73
	v_sub_f32_e32 v12, v10, v12
	v_exp_f32_e32 v13, v13
	v_mul_f32_e32 v12, 0x3fb8aa3b, v12
	v_exp_f32_e32 v12, v12
	v_mul_f32_e32 v14, 0x3fb8aa3b, v72
	v_sub_f32_e32 v13, 1.0, v13
	v_exp_f32_e32 v14, v14
	v_mul_f32_e32 v12, v13, v12
	v_add_f32_e32 v13, v15, v11
	v_sub_f32_e32 v13, v10, v13
	v_mul_f32_e32 v13, 0x3fb8aa3b, v13
	v_exp_f32_e32 v13, v13
	v_cvt_pk_bf16_f32 v12, v12, v21
	ds_write_b16 v41, v12
	v_sub_f32_e32 v12, 1.0, v14
	v_mul_f32_e32 v12, v12, v13
	v_add_f32_e32 v13, v16, v11
	v_mul_f32_e32 v14, 0x3fb8aa3b, v71
	v_sub_f32_e32 v13, v10, v13
	v_exp_f32_e32 v14, v14
	v_mul_f32_e32 v13, 0x3fb8aa3b, v13
	v_exp_f32_e32 v13, v13
	v_cvt_pk_bf16_f32 v12, v12, v21
	ds_write_b16 v41, v12 offset:272
	v_sub_f32_e32 v12, 1.0, v14
	v_mul_f32_e32 v12, v12, v13
	v_add_f32_e32 v13, v17, v11
	v_mul_f32_e32 v14, 0x3fb8aa3b, v70
	v_sub_f32_e32 v13, v10, v13
	v_exp_f32_e32 v14, v14
	v_mul_f32_e32 v13, 0x3fb8aa3b, v13
	v_exp_f32_e32 v13, v13
	v_cvt_pk_bf16_f32 v12, v12, v21
	ds_write_b16 v41, v12 offset:544
	v_sub_f32_e32 v12, 1.0, v14
	v_mul_f32_e32 v12, v12, v13
	v_add_f32_e32 v13, v74, v11
	v_mul_f32_e32 v14, 0x3fb8aa3b, v69
	v_sub_f32_e32 v13, v10, v13
	v_exp_f32_e32 v14, v14
	v_mul_f32_e32 v13, 0x3fb8aa3b, v13
	v_exp_f32_e32 v13, v13
	v_cvt_pk_bf16_f32 v12, v12, v21
	ds_write_b16 v41, v12 offset:816
	v_sub_f32_e32 v12, 1.0, v14
	v_mul_f32_e32 v12, v12, v13
	v_add_f32_e32 v13, v75, v11
	v_mul_f32_e32 v14, 0x3fb8aa3b, v68
	v_sub_f32_e32 v13, v10, v13
	v_exp_f32_e32 v14, v14
	v_mul_f32_e32 v13, 0x3fb8aa3b, v13
	v_exp_f32_e32 v13, v13
	v_cvt_pk_bf16_f32 v12, v12, v21
	ds_write_b16 v41, v12 offset:1088
	v_sub_f32_e32 v12, 1.0, v14
	v_mul_f32_e32 v12, v12, v13
	v_add_f32_e32 v13, v76, v11
	v_mul_f32_e32 v14, 0x3fb8aa3b, v67
	v_sub_f32_e32 v13, v10, v13
	v_exp_f32_e32 v14, v14
	v_mul_f32_e32 v13, 0x3fb8aa3b, v13
	v_exp_f32_e32 v13, v13
	v_cvt_pk_bf16_f32 v12, v12, v21
	ds_write_b16 v41, v12 offset:1360
	v_sub_f32_e32 v12, 1.0, v14
	v_mul_f32_e32 v12, v12, v13
	v_add_f32_e32 v13, v77, v11
	v_mul_f32_e32 v14, 0x3fb8aa3b, v66
	v_sub_f32_e32 v13, v10, v13
	v_exp_f32_e32 v14, v14
	v_mul_f32_e32 v13, 0x3fb8aa3b, v13
	v_exp_f32_e32 v13, v13
	v_cvt_pk_bf16_f32 v12, v12, v21
	ds_write_b16 v41, v12 offset:1632
	v_sub_f32_e32 v12, 1.0, v14
	v_mul_f32_e32 v12, v12, v13
	v_add_f32_e32 v13, v78, v11
	v_mul_f32_e32 v14, 0x3fb8aa3b, v65
	v_sub_f32_e32 v13, v10, v13
	v_exp_f32_e32 v14, v14
	v_mul_f32_e32 v13, 0x3fb8aa3b, v13
	v_exp_f32_e32 v13, v13
	v_cvt_pk_bf16_f32 v12, v12, v21
	ds_write_b16 v41, v12 offset:1904
	v_sub_f32_e32 v12, 1.0, v14
	v_mul_f32_e32 v12, v12, v13
	v_add_f32_e32 v13, v79, v11
	v_mul_f32_e32 v14, 0x3fb8aa3b, v64
	v_sub_f32_e32 v13, v10, v13
	v_exp_f32_e32 v14, v14
	v_mul_f32_e32 v13, 0x3fb8aa3b, v13
	v_exp_f32_e32 v13, v13
	v_cvt_pk_bf16_f32 v12, v12, v21
	ds_write_b16 v41, v12 offset:2176
	v_sub_f32_e32 v12, 1.0, v14
	v_mul_f32_e32 v12, v12, v13
	v_add_f32_e32 v13, v80, v11
	v_mul_f32_e32 v14, 0x3fb8aa3b, v63
	v_sub_f32_e32 v13, v10, v13
	v_exp_f32_e32 v14, v14
	v_mul_f32_e32 v13, 0x3fb8aa3b, v13
	v_exp_f32_e32 v13, v13
	v_cvt_pk_bf16_f32 v12, v12, v21
	ds_write_b16 v41, v12 offset:2448
	v_sub_f32_e32 v12, 1.0, v14
	v_mul_f32_e32 v12, v12, v13
	v_add_f32_e32 v13, v81, v11
	v_mul_f32_e32 v14, 0x3fb8aa3b, v62
	v_sub_f32_e32 v13, v10, v13
	v_exp_f32_e32 v14, v14
	v_mul_f32_e32 v13, 0x3fb8aa3b, v13
	v_exp_f32_e32 v13, v13
	v_cvt_pk_bf16_f32 v12, v12, v21
	ds_write_b16 v41, v12 offset:2720
	v_sub_f32_e32 v12, 1.0, v14
	v_mul_f32_e32 v12, v12, v13
	v_add_f32_e32 v13, v82, v11
	v_mul_f32_e32 v14, 0x3fb8aa3b, v61
	v_sub_f32_e32 v13, v10, v13
	v_exp_f32_e32 v14, v14
	v_mul_f32_e32 v13, 0x3fb8aa3b, v13
	v_exp_f32_e32 v13, v13
	v_cvt_pk_bf16_f32 v12, v12, v21
	ds_write_b16 v41, v12 offset:2992
	v_sub_f32_e32 v12, 1.0, v14
	v_mul_f32_e32 v12, v12, v13
	v_add_f32_e32 v13, v83, v11
	v_mul_f32_e32 v14, 0x3fb8aa3b, v60
	v_sub_f32_e32 v13, v10, v13
	v_exp_f32_e32 v14, v14
	v_mul_f32_e32 v13, 0x3fb8aa3b, v13
	v_exp_f32_e32 v13, v13
	v_cvt_pk_bf16_f32 v12, v12, v21
	ds_write_b16 v41, v12 offset:3264
	v_sub_f32_e32 v12, 1.0, v14
	v_mul_f32_e32 v12, v12, v13
	v_add_f32_e32 v13, v84, v11
	v_mul_f32_e32 v14, 0x3fb8aa3b, v59
	v_sub_f32_e32 v13, v10, v13
	v_exp_f32_e32 v14, v14
	v_mul_f32_e32 v13, 0x3fb8aa3b, v13
	v_exp_f32_e32 v13, v13
	v_cvt_pk_bf16_f32 v12, v12, v21
	ds_write_b16 v41, v12 offset:3536
	v_sub_f32_e32 v12, 1.0, v14
	v_add_f32_e32 v11, v85, v11
	v_mul_f32_e32 v12, v12, v13
	v_mul_f32_e32 v13, 0x3fb8aa3b, v58
	v_sub_f32_e32 v11, v10, v11
	v_exp_f32_e32 v13, v13
	v_mul_f32_e32 v11, 0x3fb8aa3b, v11
	v_exp_f32_e32 v11, v11
	v_cvt_pk_bf16_f32 v12, v12, v21
	ds_write_b16 v41, v12 offset:3808
	v_sub_f32_e32 v12, 1.0, v13
	v_mul_f32_e32 v11, v12, v11
	v_cvt_pk_bf16_f32 v11, v11, v21
	ds_write_b16 v41, v11 offset:4080
	s_and_saveexec_b64 s[30:31], s[12:13]
	s_cbranch_execz .LBB0_730
	v_mul_f32_e32 v10, 0x3fb8aa3b, v10
	v_exp_f32_e32 v12, v10
	v_lshl_add_u64 v[10:11], s[16:17], 0, v[26:27]
	global_store_dword v[10:11], v12, off
	s_branch .LBB0_730

; #define GAS __attribute__((address_space(1)))
; #define LDS_BARRIER() asm volatile("s_waitcnt lgkmcnt(0)\n\ts_barrier" ::: "memory")
; __device__ __forceinline__ unsigned cvt_pk_bf16(float lo, float hi) { unsigned r; asm volatile("v_cvt_pk_bf16_f32 %0, %1, %2" : "=v"(r) : "v"(lo), "v"(hi)); return r; }
; #define PHASE_IDS() int tid = threadIdx.x; asm volatile("" : "+v"(tid)); const int lane = tid & 63, w = __builtin_amdgcn_readfirstlane(tid >> 6); (void)lane; (void)w
; __device__ __forceinline__ void h3_item(Frame& F, int chunk, const GAS float* normg, int tid, const H3Regs& R) {
;     ...
;     ss += __shfl_xor(ss, 16); ss += __shfl_xor(ss, 32);
;     if (g == 0) RS[vh * 64 + 16 * tb + i] = ss;
;     LDS_BARRIER();
;     const float tot = RS[16 * tb + i] + RS[64 + 16 * tb + i];
;     const float rinv = rsqrtf(tot * (1.0f / 128.0f) + NORM_EPS);
; #pragma unroll
;     for (int vb = 0; vb < 4; ++vb) { const int vv = 16 * (4 * vh + vb) + 4 * g;
;         const f32x4 ng = ngv[vb]; const u32x2 gt = gtv[vb];
;         u32x2 wv; wv.x = cvt_pk_bf16(o[vb][0] * rinv * ng[0] * bflo(gt.x), o[vb][1] * rinv * ng[1] * bfhi(gt.x)); wv.y = cvt_pk_bf16(o[vb][2] * rinv * ng[2] * bflo(gt.y), o[vb][3] * rinv * ng[3] * bfhi(gt.y));
;         *(GAS u32x2*)(HGO + tok * HG_WIDTH + head * 128 + vv) = wv; }
;     LDS_BARRIER();
; template <int layer>
; __device__ __forceinline__ void run_layer(const Frame& F0, const XcdBarrier& bar, const int lo, const int hi) {
;     ...
;             { PHASE_IDS(); H3Regs ra, rb; int it = F.bid;
;               if (it < NCHUNK * HG_HEADS) h3_load(F, it, tid, ra);
;               for (; it < NCHUNK * HG_HEADS; it += F.G) { const int itn = it + F.G; if (itn < NCHUNK * HG_HEADS) h3_load(F, itn, tid, rb); h3_item(F, it, normg, tid, ra); ra = rb; } }
.LBB0_950:
	s_or_b64 exec, exec, s[22:23]
	s_waitcnt lgkmcnt(0)
	s_barrier
	v_lshl_add_u32 v58, s49, 2, v114
	s_waitcnt lgkmcnt(0)
	ds_read2st64_b32 v[58:59], v58 offset1:1
	v_lshlrev_b64 v[60:61], 11, v[96:97]
	s_lshl_b32 s22, s39, 7
	s_lshl_b32 s28, s22, 1
	s_add_i32 s2, s2, s42
	s_waitcnt lgkmcnt(0)
	v_add_f32_e32 v58, v58, v59
	v_fmamk_f32 v58, v58, 0x3c000000, v120
	v_mul_f32_e32 v59, 0x4b800000, v58
	v_cmp_gt_f32_e32 vcc, s48, v58
	s_add_i32 s1, s1, s43
	s_add_i32 s44, s44, s45
	v_cndmask_b32_e32 v58, v58, v59, vcc
	v_rsq_f32_e32 v62, v58
	v_lshl_add_u64 v[58:59], s[36:37], 0, v[60:61]
	v_lshl_add_u64 v[58:59], v[58:59], 0, s[28:29]
	s_mov_b32 s22, s38
	v_mul_f32_e32 v60, 0x45800000, v62
	v_cndmask_b32_e32 v60, v62, v60, vcc
	v_mul_f32_e32 v42, v42, v60
	s_waitcnt vmcnt(7)
	v_mul_f32_e32 v38, v38, v42
	s_waitcnt vmcnt(3)
	v_lshlrev_b32_e32 v42, 16, v98
	v_mul_f32_e32 v38, v38, v42
	v_mul_f32_e32 v42, v43, v60
	v_mul_f32_e32 v39, v39, v42
	v_and_b32_e32 v42, 0xffff0000, v98
	v_mul_f32_e32 v39, v39, v42
	v_cvt_pk_bf16_f32 v38, v38, v39
	v_mul_f32_e32 v39, v44, v60
	v_mul_f32_e32 v39, v40, v39
	v_lshlrev_b32_e32 v40, 16, v99
	v_mul_f32_e32 v39, v39, v40
	v_mul_f32_e32 v40, v45, v60
	v_mul_f32_e32 v40, v41, v40
	v_and_b32_e32 v41, 0xffff0000, v99
	v_mul_f32_e32 v40, v40, v41
	v_cvt_pk_bf16_f32 v39, v39, v40
	v_lshl_add_u64 v[40:41], v[92:93], 1, v[58:59]
	global_store_dwordx2 v[40:41], v[38:39], off
	v_mul_f32_e32 v38, v46, v60
	v_mul_f32_e32 v34, v34, v38
	s_waitcnt vmcnt(3)
	v_lshlrev_b32_e32 v38, 16, v94
	v_mul_f32_e32 v34, v34, v38
	v_mul_f32_e32 v38, v47, v60
	v_mul_f32_e32 v35, v35, v38
	v_and_b32_e32 v38, 0xffff0000, v94
	v_mul_f32_e32 v35, v35, v38
	v_cvt_pk_bf16_f32 v34, v34, v35
	v_mul_f32_e32 v35, v48, v60
	v_mul_f32_e32 v35, v36, v35
	v_lshlrev_b32_e32 v36, 16, v95
	v_mul_f32_e32 v35, v35, v36
	v_mul_f32_e32 v36, v49, v60
	v_mul_f32_e32 v36, v37, v36
	v_and_b32_e32 v37, 0xffff0000, v95
	v_mul_f32_e32 v36, v36, v37
	v_cvt_pk_bf16_f32 v35, v35, v36
	global_store_dwordx2 v[40:41], v[34:35], off offset:32
	v_mul_f32_e32 v34, v50, v60
	v_mul_f32_e32 v30, v30, v34
	s_waitcnt vmcnt(3)
	v_lshlrev_b32_e32 v34, 16, v90
	v_mul_f32_e32 v30, v30, v34
	v_mul_f32_e32 v34, v51, v60
	v_mul_f32_e32 v31, v31, v34
	v_and_b32_e32 v34, 0xffff0000, v90
	v_mul_f32_e32 v31, v31, v34
	v_cvt_pk_bf16_f32 v30, v30, v31
	v_mul_f32_e32 v31, v52, v60
	v_mul_f32_e32 v31, v32, v31
	v_lshlrev_b32_e32 v32, 16, v91
	v_mul_f32_e32 v31, v31, v32
	v_mul_f32_e32 v32, v53, v60
	v_mul_f32_e32 v32, v33, v32
	v_and_b32_e32 v33, 0xffff0000, v91
	v_mul_f32_e32 v32, v32, v33
	v_cvt_pk_bf16_f32 v31, v31, v32
	global_store_dwordx2 v[40:41], v[30:31], off offset:64
	v_mul_f32_e32 v30, v54, v60
	v_mul_f32_e32 v26, v26, v30
	s_waitcnt vmcnt(3)
	v_lshlrev_b32_e32 v30, 16, v88
	v_mul_f32_e32 v26, v26, v30
	v_mul_f32_e32 v30, v55, v60
	v_mul_f32_e32 v27, v27, v30
	v_and_b32_e32 v30, 0xffff0000, v88
	v_mul_f32_e32 v27, v27, v30
	v_cvt_pk_bf16_f32 v26, v26, v27
	v_mul_f32_e32 v27, v56, v60
	v_mul_f32_e32 v27, v28, v27
	v_lshlrev_b32_e32 v28, 16, v89
	v_mul_f32_e32 v27, v27, v28
	v_mul_f32_e32 v28, v57, v60
	v_mul_f32_e32 v28, v29, v28
	v_and_b32_e32 v29, 0xffff0000, v89
	v_mul_f32_e32 v28, v28, v29
	v_cvt_pk_bf16_f32 v27, v27, v28
	global_store_dwordx2 v[40:41], v[26:27], off offset:96
	s_waitcnt lgkmcnt(0)
	s_barrier
	s_waitcnt vmcnt(8)
	v_cvt_f32_f16_e32 v138, v202
	v_cvt_f32_f16_e32 v139, v203
	v_cvt_f32_f16_e32 v140, v204
	v_cvt_f32_f16_e32 v141, v205
	v_cvt_f32_f16_e32 v142, v206
	v_cvt_f32_f16_e32 v143, v207
	v_cvt_f32_f16_e32 v144, v208
	v_cvt_f32_f16_e32 v145, v209
	v_cvt_f32_f16_e32 v146, v210
	v_cvt_f32_f16_e32 v147, v211
	v_cvt_f32_f16_e32 v148, v212
	v_cvt_f32_f16_e32 v149, v213
	v_cvt_f32_f16_e32 v150, v214
	v_cvt_f32_f16_e32 v151, v215
	v_cvt_f32_f16_e32 v152, v216
	v_cvt_f32_f16_e32 v153, v217
	v_mov_b64_e32 v[44:45], v[12:13]
	v_mov_b64_e32 v[48:49], v[16:17]
	v_mov_b64_e32 v[52:53], v[4:5]
	v_mov_b64_e32 v[56:57], v[8:9]
	v_mov_b64_e32 v[60:61], v[20:21]
	v_mov_b64_e32 v[64:65], v[24:25]
	s_andn2_b64 vcc, exec, s[40:41]
	v_mov_b32_e32 v165, v138
	v_mov_b32_e32 v164, v139
	v_mov_b32_e32 v163, v140
	v_mov_b32_e32 v162, v141
	v_mov_b32_e32 v161, v142
	v_mov_b32_e32 v160, v143
	v_mov_b32_e32 v159, v144
	v_mov_b32_e32 v158, v145
	v_mov_b32_e32 v157, v146
	v_mov_b32_e32 v156, v147
	v_mov_b32_e32 v155, v148
	v_mov_b32_e32 v154, v149
	v_mov_b32_e32 v69, v150
	v_mov_b32_e32 v68, v151
	v_mov_b32_e32 v67, v152
	v_mov_b32_e32 v66, v153
	v_mov_b32_e32 v167, v122
	v_mov_b32_e32 v168, v123
	v_mov_b32_e32 v169, v124
	v_mov_b32_e32 v170, v125
	v_mov_b32_e32 v171, v126
	v_mov_b32_e32 v172, v127
	v_mov_b32_e32 v174, v128
	v_mov_b32_e32 v176, v129
	v_mov_b32_e32 v178, v130
	v_mov_b32_e32 v180, v131
	v_mov_b32_e32 v181, v132
	v_mov_b32_e32 v173, v133
	v_mov_b32_e32 v175, v134
	v_mov_b32_e32 v177, v135
	v_mov_b32_e32 v179, v136
	v_mov_b32_e32 v166, v137
	v_mov_b64_e32 v[42:43], v[10:11]
	v_mov_b64_e32 v[46:47], v[14:15]
	v_mov_b64_e32 v[50:51], v[2:3]
	v_mov_b64_e32 v[54:55], v[6:7]
	v_mov_b64_e32 v[58:59], v[18:19]
	v_mov_b64_e32 v[62:63], v[22:23]
	s_cbranch_vccz .LBB0_971
; #define GAS __attribute__((address_space(1)))
; __device__ __forceinline__ void h3_load(Frame& F, int chunk, int tid, H3Regs& R) {
;     const GAS bf16_t* H = (const GAS bf16_t*)(F.ws + WS_H); const GAS _Float16* LF = (const GAS _Float16*)(F.ws + WS_LF); const GAS bf16_t* SPT = (const GAS bf16_t*)(F.ws + WS_SPT);
;     const int bh = chunk >> 5, n = chunk & 31, b = bh >> 3, head = bh & 7, tok0 = b * SEQ + n * 64, kk = tid & 127, part = tid >> 7;
;     const GAS _Float16* p = LF + HOFF(head * 128, tok0 + part * 16) + kk; const GAS bf16_t* pq = H + HOFF(C_HQ + head * 128, tok0 + part * 16) + kk;
; #pragma unroll
;     for (int j = 0; j < 16; ++j) { R.lf[j] = (float)p[(size_t)j * 128]; R.q[j] = pq[(size_t)j * 128]; }
; #pragma unroll
;     for (int j = 0; j < 2; ++j) { const int c = tid + 512 * j, row = c >> 4, ch = c & 15; R.v[j] = *(const GAS u32x4*)(H + HOFF(C_HI + head * 128, tok0 + row) + ch * 8); }
; #pragma unroll
;     for (int j = 0; j < 4; ++j) { const int c = tid + 512 * j, row = c >> 4, ch = c & 15; R.sp[j] = *(const GAS u32x4*)(SPT + (size_t)chunk * 16384 + row * 128 + ch * 8); }
; }
.LBB0_951:
	s_add_i32 s38, s22, s0
	s_cmpk_gt_i32 s38, 0x7ff
	s_cselect_b64 s[40:41], -1, 0
	s_and_b64 vcc, exec, s[40:41]
	s_cbranch_vccnz .Lpfdrain_h3L0
	s_add_i32 s23, s43, s1
	s_add_i32 s28, s42, s2
	s_and_b32 s23, s23, 0xfffff800
	s_and_b32 s28, s28, 0x7c0
	s_or_b32 s23, s23, s28
	v_add_u32_e32 v2, s23, v100
	s_and_b32 s28, s44, 0x1c000
	v_ashrrev_i32_e32 v3, 31, v2
	v_lshl_add_u64 v[2:3], v[2:3], 0, s[28:29]
	v_lshlrev_b64 v[2:3], 8, v[2:3]
	v_lshl_add_u64 v[4:5], v[82:83], 0, v[2:3]
	v_lshl_add_u64 v[2:3], v[84:85], 0, v[2:3]
	global_load_ushort v202, v[4:5], off
	global_load_ushort v203, v[4:5], off offset:256
	global_load_ushort v204, v[4:5], off offset:512
	global_load_ushort v205, v[4:5], off offset:768
	global_load_ushort v206, v[4:5], off offset:1024
	global_load_ushort v207, v[4:5], off offset:1280
	global_load_ushort v208, v[4:5], off offset:1536
	global_load_ushort v209, v[4:5], off offset:1792
	global_load_ushort v122, v[2:3], off
	global_load_ushort v123, v[2:3], off offset:256
	global_load_ushort v124, v[2:3], off offset:512
	global_load_ushort v125, v[2:3], off offset:768
	global_load_ushort v126, v[2:3], off offset:1024
	global_load_ushort v127, v[2:3], off offset:1280
	global_load_ushort v128, v[2:3], off offset:1536
	global_load_ushort v129, v[2:3], off offset:1792
	global_load_ushort v210, v[4:5], off offset:2048
	global_load_ushort v211, v[4:5], off offset:2304
	global_load_ushort v212, v[4:5], off offset:2560
	global_load_ushort v213, v[4:5], off offset:2816
	global_load_ushort v214, v[4:5], off offset:3072
	global_load_ushort v215, v[4:5], off offset:3328
	global_load_ushort v216, v[4:5], off offset:3584
	global_load_ushort v217, v[4:5], off offset:3840
	global_load_ushort v130, v[2:3], off offset:2048
	global_load_ushort v131, v[2:3], off offset:2304
	global_load_ushort v132, v[2:3], off offset:2560
	global_load_ushort v133, v[2:3], off offset:2816
	global_load_ushort v134, v[2:3], off offset:3072
	global_load_ushort v135, v[2:3], off offset:3328
	global_load_ushort v136, v[2:3], off offset:3584
	global_load_ushort v137, v[2:3], off offset:3840
	v_add_u32_e32 v2, s23, v101
	s_bitset1_b32 s28, 18
	v_ashrrev_i32_e32 v3, 31, v2
	v_lshl_add_u64 v[2:3], v[2:3], 0, s[28:29]
	v_lshlrev_b64 v[2:3], 8, v[2:3]
	v_lshl_add_u64 v[10:11], v[74:75], 0, v[2:3]
	v_add_u32_e32 v2, s23, v102
	v_ashrrev_i32_e32 v3, 31, v2
	s_ashr_i32 s39, s38, 31
	v_lshl_add_u64 v[2:3], v[2:3], 0, s[28:29]
	s_lshl_b64 s[50:51], s[38:39], 15
	v_lshlrev_b64 v[2:3], 8, v[2:3]
	v_lshl_add_u64 v[12:13], v[86:87], 0, s[50:51]
	v_lshl_add_u64 v[14:15], v[74:75], 0, v[2:3]
	v_lshl_add_u64 v[2:3], v[72:73], 1, v[12:13]
	v_lshl_add_u64 v[6:7], v[76:77], 1, v[12:13]
	v_lshl_add_u64 v[16:17], v[78:79], 1, v[12:13]
	v_lshl_add_u64 v[12:13], v[80:81], 1, v[12:13]
	global_load_dwordx4 v[2:5], v[2:3], off
	s_nop 0
	global_load_dwordx4 v[6:9], v[6:7], off
	s_nop 0
	global_load_dwordx4 v[18:21], v[16:17], off
	global_load_dwordx4 v[22:25], v[12:13], off
	s_nop 0
	global_load_dwordx4 v[10:13], v[10:11], off
	s_nop 0
	global_load_dwordx4 v[14:17], v[14:15], off
	s_waitcnt vmcnt(38)
	s_branch .LBB0_953

; #define GAS __attribute__((address_space(1)))
; #define LAS __attribute__((address_space(3)))
; #define LDS_BARRIER() asm volatile("s_waitcnt lgkmcnt(0)\n\ts_barrier" ::: "memory")
; __device__ __forceinline__ void h3_item(Frame& F, int chunk, const GAS float* normg, int tid, const H3Regs& R) {
;     const GAS bf16_t* H = (const GAS bf16_t*)(F.ws + WS_H); GAS bf16_t* HGO = (GAS bf16_t*)(F.ws + WS_HGO);
;     const int bh = chunk >> 5, n = chunk & 31, b = bh >> 3, head = bh & 7, tok0 = b * SEQ + n * 64;
;     LAS unsigned char* QT = F.lds; LAS unsigned char* QH = F.lds + 17408; LAS unsigned char* KH = F.lds + 34816; LAS unsigned char* VT = F.lds + 52224; LAS unsigned char* SP = F.lds + 69632;
;     LAS float* TOT = (LAS float*)(F.lds + 104448); LAS float* RS = (LAS float*)(F.lds + 106496);
;     const int lane = tid & 63, w = __builtin_amdgcn_readfirstlane(tid >> 6);
;     const int kk = tid & 127, part = tid >> 7, g = lane >> 4, i = lane & 15;
;     const int tb = w & 3, vh = w >> 2;
;     const size_t tok = (size_t)(tok0 + 16 * tb + i);
;     f32x4 ngv[4]; u32x2 gtv[4];
; #pragma unroll
;     for (int vb = 0; vb < 4; ++vb) { const int vv = 16 * (4 * vh + vb) + 4 * g; ngv[vb] = *(const GAS f32x4*)(normg + head * 128 + vv); gtv[vb] = *(const GAS u32x2*)(H + HOFF(C_HGATE + head * 128, tok) + vv); }
;     float lf[16], cum[16], qv[16];
; #pragma unroll
;     for (int j = 0; j < 16; ++j) { lf[j] = R.lf[j]; qv[j] = bf2f(R.q[j]); }
; #pragma unroll
;     for (int j = 0; j < 2; ++j) { const int c = tid + 512 * j, row = c >> 4, ch = c & 15; *(LAS u32x4*)(VT + row * TROW + ch * 16) = R.v[j]; }
; #pragma unroll
;     for (int j = 0; j < 4; ++j) { const int c = tid + 512 * j, row = c >> 4, ch = c & 15; *(LAS u32x4*)(SP + row * TROW + ch * 16) = R.sp[j]; }
;     float run = 0.f;
; #pragma unroll
;     for (int j = 0; j < 16; ++j) { run += lf[j]; cum[j] = run; }
;     TOT[part * 128 + kk] = run;
;     LDS_BARRIER();
.LBB0_953:
	s_bfe_u32 s39, s22, 0x30005
	s_and_b32 s22, s1, 0xfffff800
	s_and_b32 s23, s2, 0x7c0
	v_readfirstlane_b32 s50, v1
	s_bfe_u32 s57, s50, 0x20006
	s_ashr_i32 s56, s50, 8
	s_or_b32 s22, s23, s22
	s_lshl_b32 s49, s57, 4
	v_or_b32_e32 v26, s22, v103
	s_lshl_b32 s51, s56, 6
	s_lshl_b32 s22, s39, 9
	s_waitcnt lgkmcnt(0)
	s_add_u32 s22, s34, s22
	v_or_b32_e32 v96, s49, v26
	s_addc_u32 s23, s35, 0
	s_lshl_b32 s28, s39, 14
	v_ashrrev_i32_e32 v97, 31, v96
	s_or_b32 s28, s28, 0x60000
	v_lshl_add_u64 v[26:27], v[96:97], 0, s[28:29]
	v_or_b32_e32 v92, s51, v104
	v_lshlrev_b64 v[26:27], 8, v[26:27]
	v_lshl_add_u64 v[26:27], s[30:31], 0, v[26:27]
	v_ashrrev_i32_e32 v93, 31, v92
	v_lshl_add_u64 v[28:29], v[92:93], 2, s[22:23]
	v_lshl_add_u64 v[88:89], v[92:93], 1, v[26:27]
	global_load_dwordx4 v[38:41], v[28:29], off
	global_load_dwordx4 v[34:37], v[28:29], off offset:64
	global_load_dwordx4 v[30:33], v[28:29], off offset:128
	s_nop 0
	global_load_dwordx4 v[26:29], v[28:29], off offset:192
	s_nop 0
	global_load_dwordx2 v[98:99], v[88:89], off
	global_load_dwordx2 v[94:95], v[88:89], off offset:32
	global_load_dwordx2 v[90:91], v[88:89], off offset:64
	s_nop 0
	global_load_dwordx2 v[88:89], v[88:89], off offset:96
	v_add_u32_e32 v182, v105, v106
	ds_write_b128 v182, v[42:45] offset:52224
	v_add_u32_e32 v42, v105, v107
	ds_write_b128 v42, v[46:49] offset:52224
	v_add_u32_e32 v42, v108, v106
	ds_write_b128 v42, v[50:53]
	v_add_u32_e32 v42, v108, v107
	ds_write_b128 v42, v[54:57]
	ds_write_b128 v116, v[58:61]
	ds_write_b128 v117, v[62:65]
	v_add_f32_e32 v58, 0, v165
	v_add_f32_e32 v57, v164, v58
	v_add_f32_e32 v56, v163, v57
	v_add_f32_e32 v55, v162, v56
	v_add_f32_e32 v54, v161, v55
	v_add_f32_e32 v53, v160, v54
	v_add_f32_e32 v52, v159, v53
	v_add_f32_e32 v51, v158, v52
	v_add_f32_e32 v50, v157, v51
	v_add_f32_e32 v49, v156, v50
	v_add_f32_e32 v48, v155, v49
	v_add_f32_e32 v47, v154, v48
	v_add_f32_e32 v46, v69, v47
	v_add_f32_e32 v45, v68, v46
	v_add_f32_e32 v44, v67, v45
	v_add_f32_e32 v43, v66, v44
	ds_write_b32 v109, v43
	s_waitcnt lgkmcnt(0)
	s_barrier
	v_mov_b32_e32 v42, 0
	s_and_saveexec_b64 s[22:23], s[4:5]
	s_cbranch_execz .LBB0_957
	ds_read_b32 v42, v110
	s_waitcnt lgkmcnt(0)
	v_add_f32_e32 v42, 0, v42
	s_or_b64 exec, exec, s[22:23]
	s_and_saveexec_b64 s[22:23], s[6:7]
	s_cbranch_execnz .LBB0_958

; #define GAS __attribute__((address_space(1)))
; #define LDS_BARRIER() asm volatile("s_waitcnt lgkmcnt(0)\n\ts_barrier" ::: "memory")
; __device__ __forceinline__ unsigned cvt_pk_bf16(float lo, float hi) { unsigned r; asm volatile("v_cvt_pk_bf16_f32 %0, %1, %2" : "=v"(r) : "v"(lo), "v"(hi)); return r; }
; __device__ __forceinline__ void h3_item(Frame& F, int chunk, const GAS float* normg, int tid, const H3Regs& R) {
;     ...
;     if (g == 0) RS[vh * 64 + 16 * tb + i] = ss;
;     LDS_BARRIER();
;     const float tot = RS[16 * tb + i] + RS[64 + 16 * tb + i];
;     const float rinv = rsqrtf(tot * (1.0f / 128.0f) + NORM_EPS);
; #pragma unroll
;     for (int vb = 0; vb < 4; ++vb) { const int vv = 16 * (4 * vh + vb) + 4 * g;
;         const f32x4 ng = ngv[vb]; const u32x2 gt = gtv[vb];
;         u32x2 wv; wv.x = cvt_pk_bf16(o[vb][0] * rinv * ng[0] * bflo(gt.x), o[vb][1] * rinv * ng[1] * bfhi(gt.x)); wv.y = cvt_pk_bf16(o[vb][2] * rinv * ng[2] * bflo(gt.y), o[vb][3] * rinv * ng[3] * bfhi(gt.y));
;         *(GAS u32x2*)(HGO + tok * HG_WIDTH + head * 128 + vv) = wv; }
;     LDS_BARRIER();
; template <int layer>
; __device__ __forceinline__ void run_layer(const Frame& F0, const XcdBarrier& bar, const int lo, const int hi) {
;     ...
;               for (; it < NCHUNK * HG_HEADS; it += F.G) { const int itn = it + F.G; if (itn < NCHUNK * HG_HEADS) h3_load(F, itn, tid, rb); h3_item(F, it, normg, tid, ra); ra = rb; } }
.LBB0_2515:
	s_or_b64 exec, exec, s[22:23]
	s_waitcnt lgkmcnt(0)
	s_barrier
	v_lshl_add_u32 v58, s49, 2, v114
	s_waitcnt lgkmcnt(0)
	ds_read2st64_b32 v[58:59], v58 offset1:1
	v_lshlrev_b64 v[60:61], 11, v[96:97]
	s_lshl_b32 s22, s37, 7
	s_lshl_b32 s28, s22, 1
	s_add_i32 s24, s24, s42
	s_waitcnt lgkmcnt(0)
	v_add_f32_e32 v58, v58, v59
	v_fmamk_f32 v58, v58, 0x3c000000, v120
	v_mul_f32_e32 v59, 0x4b800000, v58
	v_cmp_gt_f32_e32 vcc, s48, v58
	s_add_i32 s3, s3, s43
	s_add_i32 s44, s44, s45
	v_cndmask_b32_e32 v58, v58, v59, vcc
	v_rsq_f32_e32 v62, v58
	v_lshl_add_u64 v[58:59], s[34:35], 0, v[60:61]
	v_lshl_add_u64 v[58:59], v[58:59], 0, s[28:29]
	s_mov_b32 s22, s36
	v_mul_f32_e32 v60, 0x45800000, v62
	v_cndmask_b32_e32 v60, v62, v60, vcc
	v_mul_f32_e32 v42, v42, v60
	s_waitcnt vmcnt(7)
	v_mul_f32_e32 v38, v38, v42
	s_waitcnt vmcnt(3)
	v_lshlrev_b32_e32 v42, 16, v98
	v_mul_f32_e32 v38, v38, v42
	v_mul_f32_e32 v42, v43, v60
	v_mul_f32_e32 v39, v39, v42
	v_and_b32_e32 v42, 0xffff0000, v98
	v_mul_f32_e32 v39, v39, v42
	v_cvt_pk_bf16_f32 v38, v38, v39
	v_mul_f32_e32 v39, v44, v60
	v_mul_f32_e32 v39, v40, v39
	v_lshlrev_b32_e32 v40, 16, v99
	v_mul_f32_e32 v39, v39, v40
	v_mul_f32_e32 v40, v45, v60
	v_mul_f32_e32 v40, v41, v40
	v_and_b32_e32 v41, 0xffff0000, v99
	v_mul_f32_e32 v40, v40, v41
	v_cvt_pk_bf16_f32 v39, v39, v40
	v_lshl_add_u64 v[40:41], v[92:93], 1, v[58:59]
	global_store_dwordx2 v[40:41], v[38:39], off
	v_mul_f32_e32 v38, v46, v60
	v_mul_f32_e32 v34, v34, v38
	s_waitcnt vmcnt(3)
	v_lshlrev_b32_e32 v38, 16, v94
	v_mul_f32_e32 v34, v34, v38
	v_mul_f32_e32 v38, v47, v60
	v_mul_f32_e32 v35, v35, v38
	v_and_b32_e32 v38, 0xffff0000, v94
	v_mul_f32_e32 v35, v35, v38
	v_cvt_pk_bf16_f32 v34, v34, v35
	v_mul_f32_e32 v35, v48, v60
	v_mul_f32_e32 v35, v36, v35
	v_lshlrev_b32_e32 v36, 16, v95
	v_mul_f32_e32 v35, v35, v36
	v_mul_f32_e32 v36, v49, v60
	v_mul_f32_e32 v36, v37, v36
	v_and_b32_e32 v37, 0xffff0000, v95
	v_mul_f32_e32 v36, v36, v37
	v_cvt_pk_bf16_f32 v35, v35, v36
	global_store_dwordx2 v[40:41], v[34:35], off offset:32
	v_mul_f32_e32 v34, v50, v60
	v_mul_f32_e32 v30, v30, v34
	s_waitcnt vmcnt(3)
	v_lshlrev_b32_e32 v34, 16, v90
	v_mul_f32_e32 v30, v30, v34
	v_mul_f32_e32 v34, v51, v60
	v_mul_f32_e32 v31, v31, v34
	v_and_b32_e32 v34, 0xffff0000, v90
	v_mul_f32_e32 v31, v31, v34
	v_cvt_pk_bf16_f32 v30, v30, v31
	v_mul_f32_e32 v31, v52, v60
	v_mul_f32_e32 v31, v32, v31
	v_lshlrev_b32_e32 v32, 16, v91
	v_mul_f32_e32 v31, v31, v32
	v_mul_f32_e32 v32, v53, v60
	v_mul_f32_e32 v32, v33, v32
	v_and_b32_e32 v33, 0xffff0000, v91
	v_mul_f32_e32 v32, v32, v33
	v_cvt_pk_bf16_f32 v31, v31, v32
	global_store_dwordx2 v[40:41], v[30:31], off offset:64
	v_mul_f32_e32 v30, v54, v60
	v_mul_f32_e32 v26, v26, v30
	s_waitcnt vmcnt(3)
	v_lshlrev_b32_e32 v30, 16, v88
	v_mul_f32_e32 v26, v26, v30
	v_mul_f32_e32 v30, v55, v60
	v_mul_f32_e32 v27, v27, v30
	v_and_b32_e32 v30, 0xffff0000, v88
	v_mul_f32_e32 v27, v27, v30
	v_cvt_pk_bf16_f32 v26, v26, v27
	v_mul_f32_e32 v27, v56, v60
	v_mul_f32_e32 v27, v28, v27
	v_lshlrev_b32_e32 v28, 16, v89
	v_mul_f32_e32 v27, v27, v28
	v_mul_f32_e32 v28, v57, v60
	v_mul_f32_e32 v28, v29, v28
	v_and_b32_e32 v29, 0xffff0000, v89
	v_mul_f32_e32 v28, v28, v29
	v_cvt_pk_bf16_f32 v27, v27, v28
	global_store_dwordx2 v[40:41], v[26:27], off offset:96
	s_waitcnt lgkmcnt(0)
	s_barrier
	s_waitcnt vmcnt(8)
	v_cvt_f32_f16_e32 v138, v202
	v_cvt_f32_f16_e32 v139, v203
	v_cvt_f32_f16_e32 v140, v204
	v_cvt_f32_f16_e32 v141, v205
	v_cvt_f32_f16_e32 v142, v206
	v_cvt_f32_f16_e32 v143, v207
	v_cvt_f32_f16_e32 v144, v208
	v_cvt_f32_f16_e32 v145, v209
	v_cvt_f32_f16_e32 v146, v210
	v_cvt_f32_f16_e32 v147, v211
	v_cvt_f32_f16_e32 v148, v212
	v_cvt_f32_f16_e32 v149, v213
	v_cvt_f32_f16_e32 v150, v214
	v_cvt_f32_f16_e32 v151, v215
	v_cvt_f32_f16_e32 v152, v216
	v_cvt_f32_f16_e32 v153, v217
	v_mov_b64_e32 v[44:45], v[12:13]
	v_mov_b64_e32 v[48:49], v[16:17]
	v_mov_b64_e32 v[52:53], v[4:5]
	v_mov_b64_e32 v[56:57], v[8:9]
	v_mov_b64_e32 v[60:61], v[20:21]
	v_mov_b64_e32 v[64:65], v[24:25]
	s_andn2_b64 vcc, exec, s[38:39]
	v_mov_b32_e32 v165, v138
	v_mov_b32_e32 v164, v139
	v_mov_b32_e32 v163, v140
	v_mov_b32_e32 v162, v141
	v_mov_b32_e32 v161, v142
	v_mov_b32_e32 v160, v143
	v_mov_b32_e32 v159, v144
	v_mov_b32_e32 v158, v145
	v_mov_b32_e32 v157, v146
	v_mov_b32_e32 v156, v147
	v_mov_b32_e32 v155, v148
	v_mov_b32_e32 v154, v149
	v_mov_b32_e32 v69, v150
	v_mov_b32_e32 v68, v151
	v_mov_b32_e32 v67, v152
	v_mov_b32_e32 v66, v153
	v_mov_b32_e32 v167, v122
	v_mov_b32_e32 v168, v123
	v_mov_b32_e32 v169, v124
	v_mov_b32_e32 v170, v125
	v_mov_b32_e32 v171, v126
	v_mov_b32_e32 v172, v127
	v_mov_b32_e32 v174, v128
	v_mov_b32_e32 v176, v129
	v_mov_b32_e32 v178, v130
	v_mov_b32_e32 v180, v131
	v_mov_b32_e32 v181, v132
	v_mov_b32_e32 v173, v133
	v_mov_b32_e32 v175, v134
	v_mov_b32_e32 v177, v135
	v_mov_b32_e32 v179, v136
	v_mov_b32_e32 v166, v137
	v_mov_b64_e32 v[42:43], v[10:11]
	v_mov_b64_e32 v[46:47], v[14:15]
	v_mov_b64_e32 v[50:51], v[2:3]
	v_mov_b64_e32 v[54:55], v[6:7]
	v_mov_b64_e32 v[58:59], v[18:19]
	v_mov_b64_e32 v[62:63], v[22:23]
	s_cbranch_vccz .LBB0_2536
; #define GAS __attribute__((address_space(1)))
; __device__ __forceinline__ void h3_load(Frame& F, int chunk, int tid, H3Regs& R) {
;     const GAS bf16_t* H = (const GAS bf16_t*)(F.ws + WS_H); const GAS _Float16* LF = (const GAS _Float16*)(F.ws + WS_LF); const GAS bf16_t* SPT = (const GAS bf16_t*)(F.ws + WS_SPT);
;     const int bh = chunk >> 5, n = chunk & 31, b = bh >> 3, head = bh & 7, tok0 = b * SEQ + n * 64, kk = tid & 127, part = tid >> 7;
;     const GAS _Float16* p = LF + HOFF(head * 128, tok0 + part * 16) + kk; const GAS bf16_t* pq = H + HOFF(C_HQ + head * 128, tok0 + part * 16) + kk;
; #pragma unroll
;     for (int j = 0; j < 16; ++j) { R.lf[j] = (float)p[(size_t)j * 128]; R.q[j] = pq[(size_t)j * 128]; }
; #pragma unroll
;     for (int j = 0; j < 2; ++j) { const int c = tid + 512 * j, row = c >> 4, ch = c & 15; R.v[j] = *(const GAS u32x4*)(H + HOFF(C_HI + head * 128, tok0 + row) + ch * 8); }
; #pragma unroll
;     for (int j = 0; j < 4; ++j) { const int c = tid + 512 * j, row = c >> 4, ch = c & 15; R.sp[j] = *(const GAS u32x4*)(SPT + (size_t)chunk * 16384 + row * 128 + ch * 8); }
; }
; template <int layer>
; __device__ __forceinline__ void run_layer(const Frame& F0, const XcdBarrier& bar, const int lo, const int hi) {
;     ...
;               for (; it < NCHUNK * HG_HEADS; it += F.G) { const int itn = it + F.G; if (itn < NCHUNK * HG_HEADS) h3_load(F, itn, tid, rb); h3_item(F, it, normg, tid, ra); ra = rb; } }
.LBB0_2516:
	s_add_i32 s36, s22, s0
	s_cmpk_gt_i32 s36, 0x7ff
	s_cselect_b64 s[38:39], -1, 0
	s_and_b64 vcc, exec, s[38:39]
	s_cbranch_vccnz .Lpfdrain_h3L1
	s_add_i32 s23, s43, s3
	s_add_i32 s28, s42, s24
	s_and_b32 s23, s23, 0xfffff800
	s_and_b32 s28, s28, 0x7c0
	s_or_b32 s23, s23, s28
	v_add_u32_e32 v2, s23, v100
	s_and_b32 s28, s44, 0x1c000
	v_ashrrev_i32_e32 v3, 31, v2
	v_lshl_add_u64 v[2:3], v[2:3], 0, s[28:29]
	v_lshlrev_b64 v[2:3], 8, v[2:3]
	v_lshl_add_u64 v[4:5], v[82:83], 0, v[2:3]
	v_lshl_add_u64 v[2:3], v[84:85], 0, v[2:3]
	global_load_ushort v202, v[4:5], off
	global_load_ushort v203, v[4:5], off offset:256
	global_load_ushort v204, v[4:5], off offset:512
	global_load_ushort v205, v[4:5], off offset:768
	global_load_ushort v206, v[4:5], off offset:1024
	global_load_ushort v207, v[4:5], off offset:1280
	global_load_ushort v208, v[4:5], off offset:1536
	global_load_ushort v209, v[4:5], off offset:1792
	global_load_ushort v122, v[2:3], off
	global_load_ushort v123, v[2:3], off offset:256
	global_load_ushort v124, v[2:3], off offset:512
	global_load_ushort v125, v[2:3], off offset:768
	global_load_ushort v126, v[2:3], off offset:1024
	global_load_ushort v127, v[2:3], off offset:1280
	global_load_ushort v128, v[2:3], off offset:1536
	global_load_ushort v129, v[2:3], off offset:1792
	global_load_ushort v210, v[4:5], off offset:2048
	global_load_ushort v211, v[4:5], off offset:2304
	global_load_ushort v212, v[4:5], off offset:2560
	global_load_ushort v213, v[4:5], off offset:2816
	global_load_ushort v214, v[4:5], off offset:3072
	global_load_ushort v215, v[4:5], off offset:3328
	global_load_ushort v216, v[4:5], off offset:3584
	global_load_ushort v217, v[4:5], off offset:3840
	global_load_ushort v130, v[2:3], off offset:2048
	global_load_ushort v131, v[2:3], off offset:2304
	global_load_ushort v132, v[2:3], off offset:2560
	global_load_ushort v133, v[2:3], off offset:2816
	global_load_ushort v134, v[2:3], off offset:3072
	global_load_ushort v135, v[2:3], off offset:3328
	global_load_ushort v136, v[2:3], off offset:3584
	global_load_ushort v137, v[2:3], off offset:3840
	v_add_u32_e32 v2, s23, v101
	s_bitset1_b32 s28, 18
	v_ashrrev_i32_e32 v3, 31, v2
	v_lshl_add_u64 v[2:3], v[2:3], 0, s[28:29]
	v_lshlrev_b64 v[2:3], 8, v[2:3]
	v_lshl_add_u64 v[10:11], v[76:77], 0, v[2:3]
	v_add_u32_e32 v2, s23, v102
	v_ashrrev_i32_e32 v3, 31, v2
	s_ashr_i32 s37, s36, 31
	v_lshl_add_u64 v[2:3], v[2:3], 0, s[28:29]
	s_lshl_b64 s[50:51], s[36:37], 15
	v_lshlrev_b64 v[2:3], 8, v[2:3]
	v_lshl_add_u64 v[12:13], v[86:87], 0, s[50:51]
	v_lshl_add_u64 v[14:15], v[76:77], 0, v[2:3]
	v_lshl_add_u64 v[2:3], v[72:73], 1, v[12:13]
	v_lshl_add_u64 v[6:7], v[74:75], 1, v[12:13]
	v_lshl_add_u64 v[16:17], v[78:79], 1, v[12:13]
	v_lshl_add_u64 v[12:13], v[80:81], 1, v[12:13]
	global_load_dwordx4 v[2:5], v[2:3], off
	s_nop 0
	global_load_dwordx4 v[6:9], v[6:7], off
	s_nop 0
	global_load_dwordx4 v[18:21], v[16:17], off
	global_load_dwordx4 v[22:25], v[12:13], off
	s_nop 0
	global_load_dwordx4 v[10:13], v[10:11], off
	s_nop 0
	global_load_dwordx4 v[14:17], v[14:15], off
	s_waitcnt vmcnt(38)
	s_branch .LBB0_2518

; #define GAS __attribute__((address_space(1)))
; #define LAS __attribute__((address_space(3)))
; #define LDS_BARRIER() asm volatile("s_waitcnt lgkmcnt(0)\n\ts_barrier" ::: "memory")
; __device__ __forceinline__ void h3_item(Frame& F, int chunk, const GAS float* normg, int tid, const H3Regs& R) {
;     ...
;     const size_t tok = (size_t)(tok0 + 16 * tb + i);
;     f32x4 ngv[4]; u32x2 gtv[4];
; #pragma unroll
;     for (int vb = 0; vb < 4; ++vb) { const int vv = 16 * (4 * vh + vb) + 4 * g; ngv[vb] = *(const GAS f32x4*)(normg + head * 128 + vv); gtv[vb] = *(const GAS u32x2*)(H + HOFF(C_HGATE + head * 128, tok) + vv); }
;     float lf[16], cum[16], qv[16];
; #pragma unroll
;     for (int j = 0; j < 16; ++j) { lf[j] = R.lf[j]; qv[j] = bf2f(R.q[j]); }
; #pragma unroll
;     for (int j = 0; j < 2; ++j) { const int c = tid + 512 * j, row = c >> 4, ch = c & 15; *(LAS u32x4*)(VT + row * TROW + ch * 16) = R.v[j]; }
; #pragma unroll
;     for (int j = 0; j < 4; ++j) { const int c = tid + 512 * j, row = c >> 4, ch = c & 15; *(LAS u32x4*)(SP + row * TROW + ch * 16) = R.sp[j]; }
;     float run = 0.f;
; #pragma unroll
;     for (int j = 0; j < 16; ++j) { run += lf[j]; cum[j] = run; }
;     TOT[part * 128 + kk] = run;
;     LDS_BARRIER();
.LBB0_2518:
	s_bfe_u32 s37, s22, 0x30005
	s_and_b32 s22, s3, 0xfffff800
	s_and_b32 s23, s24, 0x7c0
	v_readfirstlane_b32 s50, v1
	s_bfe_u32 s57, s50, 0x20006
	s_ashr_i32 s56, s50, 8
	s_or_b32 s22, s23, s22
	s_lshl_b32 s49, s57, 4
	v_or_b32_e32 v26, s22, v103
	s_lshl_b32 s51, s56, 6
	s_lshl_b32 s22, s37, 9
	s_add_u32 s22, s1, s22
	v_or_b32_e32 v96, s49, v26
	s_addc_u32 s23, s2, 0
	s_lshl_b32 s28, s37, 14
	v_ashrrev_i32_e32 v97, 31, v96
	s_or_b32 s28, s28, 0x60000
	v_lshl_add_u64 v[26:27], v[96:97], 0, s[28:29]
	v_or_b32_e32 v92, s51, v104
	v_lshlrev_b64 v[26:27], 8, v[26:27]
	v_lshl_add_u64 v[26:27], s[30:31], 0, v[26:27]
	v_ashrrev_i32_e32 v93, 31, v92
	v_lshl_add_u64 v[28:29], v[92:93], 2, s[22:23]
	v_lshl_add_u64 v[88:89], v[92:93], 1, v[26:27]
	global_load_dwordx4 v[38:41], v[28:29], off
	global_load_dwordx4 v[34:37], v[28:29], off offset:64
	global_load_dwordx4 v[30:33], v[28:29], off offset:128
	s_nop 0
	global_load_dwordx4 v[26:29], v[28:29], off offset:192
	s_nop 0
	global_load_dwordx2 v[98:99], v[88:89], off
	global_load_dwordx2 v[94:95], v[88:89], off offset:32
	global_load_dwordx2 v[90:91], v[88:89], off offset:64
	s_nop 0
	global_load_dwordx2 v[88:89], v[88:89], off offset:96
	v_add_u32_e32 v182, v105, v106
	ds_write_b128 v182, v[42:45] offset:52224
	v_add_u32_e32 v42, v105, v107
	ds_write_b128 v42, v[46:49] offset:52224
	v_add_u32_e32 v42, v108, v106
	ds_write_b128 v42, v[50:53]
	v_add_u32_e32 v42, v108, v107
	ds_write_b128 v42, v[54:57]
	ds_write_b128 v116, v[58:61]
	ds_write_b128 v117, v[62:65]
	v_add_f32_e32 v58, 0, v165
	v_add_f32_e32 v57, v164, v58
	v_add_f32_e32 v56, v163, v57
	v_add_f32_e32 v55, v162, v56
	v_add_f32_e32 v54, v161, v55
	v_add_f32_e32 v53, v160, v54
	v_add_f32_e32 v52, v159, v53
	v_add_f32_e32 v51, v158, v52
	v_add_f32_e32 v50, v157, v51
	v_add_f32_e32 v49, v156, v50
	v_add_f32_e32 v48, v155, v49
	v_add_f32_e32 v47, v154, v48
	v_add_f32_e32 v46, v69, v47
	v_add_f32_e32 v45, v68, v46
	v_add_f32_e32 v44, v67, v45
	v_add_f32_e32 v43, v66, v44
	ds_write_b32 v109, v43
	s_waitcnt lgkmcnt(0)
	s_barrier
	v_mov_b32_e32 v42, 0
	s_and_saveexec_b64 s[22:23], s[4:5]
	s_cbranch_execz .LBB0_2522
	ds_read_b32 v42, v110
	s_waitcnt lgkmcnt(0)
	v_add_f32_e32 v42, 0, v42
	s_or_b64 exec, exec, s[22:23]
	s_and_saveexec_b64 s[22:23], s[6:7]
	s_cbranch_execnz .LBB0_2523
